# sec 6.3(1) recipe kernel-wide: every per-phase s_setprio deleted + one static s_setprio 1 for waves 4-7 at kernel entry
# baseline (speedup 1.0000x reference)
_Z6k_mega6Params:
	v_readfirstlane_b32 s98, v0
	s_nop 3
	s_lshr_b32 s98, s98, 8
	s_cmp_lg_u32 s98, 0
	s_cbranch_scc0 .Lkprio_done
	s_setprio 1
.Lkprio_done:
	s_load_dwordx4 s[12:15], s[0:1], 0x120
	s_load_dwordx8 s[4:11], s[0:1], 0x100
	v_mov_b32_e32 v1, v0
	v_writelane_b32 v251, s2, 0
	s_waitcnt lgkmcnt(0)
	v_writelane_b32 v251, s4, 1
	v_cmp_eq_u32_e32 vcc, 0, v1
	s_nop 0
	v_writelane_b32 v251, s5, 2
	v_writelane_b32 v251, s6, 3
	v_writelane_b32 v251, s7, 4
	v_writelane_b32 v251, s8, 5
	v_writelane_b32 v251, s9, 6
	v_writelane_b32 v251, s10, 7
	v_writelane_b32 v251, s11, 8
	s_and_saveexec_b64 s[4:5], vcc
	s_cbranch_execz .LBB0_2
	s_add_i32 s2, 0, 0x23ff0
	v_mov_b32_e32 v1, 0
	v_mov_b32_e32 v2, s2
	s_add_i32 s2, 0, 0x23ff4
	ds_write_b32 v2, v1
	v_mov_b32_e32 v2, s2
	s_add_i32 s2, 0, 0x23ff8
	ds_write_b32 v2, v1
	v_mov_b32_e32 v2, s2
	s_add_i32 s2, 0, 0x23ffc
	ds_write_b32 v2, v1
	v_mov_b32_e32 v2, s2
	ds_write_b32 v2, v1
